# BG_CONV 93 so the in-projection GEMM takes 11 rounds; P5 g_hg/g_fox loads hoisted above the stores; P7 x1 row loads issued together with token-1 prefetch
# speedup vs baseline: 1.0175x; 1.0010x over previous
.LBB0_682:
	v_lshl_add_u64 v[2:3], s[76:77], 0, v[28:29]
	v_add_co_u32_e32 v30, vcc, 0x54768000, v2
	s_add_i32 s22, s14, s15
	s_nop 0
	v_addc_co_u32_e32 v31, vcc, 0, v3, vcc
	global_load_dwordx2 v[226:227], v[30:31], off
	global_load_dwordx2 v[228:229], v[30:31], off offset:512
	global_load_dwordx2 v[230:231], v[30:31], off offset:1024
	global_load_dwordx2 v[232:233], v[30:31], off offset:1536
	global_load_dwordx2 v[234:235], v[30:31], off offset:2048
	global_load_dwordx2 v[236:237], v[30:31], off offset:2560
	global_load_dwordx2 v[238:239], v[30:31], off offset:3072
	global_load_dwordx2 v[240:241], v[30:31], off offset:3584
	s_add_i32 s98, s22, 1
	s_ashr_i32 s99, s98, 31
	s_lshl_b64 s[98:99], s[98:99], 12
	v_lshl_add_u64 v[252:253], v[22:23], 0, s[98:99]
	global_load_dwordx2 v[242:243], v[252:253], off
	global_load_dwordx2 v[244:245], v[252:253], off offset:512
	global_load_dwordx2 v[246:247], v[252:253], off offset:1024
	global_load_dwordx2 v[248:249], v[252:253], off offset:1536
	global_load_dwordx2 v[250:251], v[252:253], off offset:2048
	s_ashr_i32 s0, s22, 13
	s_mulk_i32 s0, 0x3000
	s_ashr_i32 s1, s0, 31
	s_lshl_b64 s[0:1], s[0:1], 2
	s_add_u32 s20, s3, s0
	s_addc_u32 s21, s24, s1
	s_add_u32 s0, s20, 0x6000
	s_addc_u32 s1, s21, 0
	s_add_u32 s20, s20, 0x8000
	s_addc_u32 s21, s21, 0
	s_waitcnt vmcnt(12)
	v_and_b32_e32 v3, 0xffff0000, v226
	s_waitcnt vmcnt(11)
	v_and_b32_e32 v57, 0xffff0000, v228
	v_lshlrev_b32_e32 v2, 16, v226
	v_mul_f32_e32 v34, v3, v3
	v_lshlrev_b32_e32 v56, 16, v228
	v_mul_f32_e32 v32, v57, v57
	v_lshlrev_b32_e32 v4, 16, v227
	v_fmac_f32_e32 v34, v2, v2
	v_lshlrev_b32_e32 v58, 16, v229
	v_fmac_f32_e32 v32, v56, v56
	v_and_b32_e32 v5, 0xffff0000, v227
	v_fmac_f32_e32 v34, v4, v4
	v_and_b32_e32 v59, 0xffff0000, v229
	v_fmac_f32_e32 v32, v58, v58
	v_fmac_f32_e32 v34, v5, v5
	v_fmac_f32_e32 v32, v59, v59
	v_add_f32_e32 v34, v34, v32
	s_waitcnt vmcnt(10)
	v_and_b32_e32 v53, 0xffff0000, v230
	v_lshlrev_b32_e32 v52, 16, v230
	v_mul_f32_e32 v32, v53, v53
	v_lshlrev_b32_e32 v54, 16, v231
	v_fmac_f32_e32 v32, v52, v52
	v_and_b32_e32 v55, 0xffff0000, v231
	v_fmac_f32_e32 v32, v54, v54
	v_fmac_f32_e32 v32, v55, v55
	v_add_f32_e32 v34, v34, v32
	s_waitcnt vmcnt(9)
	v_and_b32_e32 v49, 0xffff0000, v232
	v_lshlrev_b32_e32 v48, 16, v232
	v_mul_f32_e32 v32, v49, v49
	v_lshlrev_b32_e32 v50, 16, v233
	v_fmac_f32_e32 v32, v48, v48
	v_and_b32_e32 v51, 0xffff0000, v233
	v_fmac_f32_e32 v32, v50, v50
	v_fmac_f32_e32 v32, v51, v51
	v_add_f32_e32 v36, v34, v32
	s_waitcnt vmcnt(8)
	v_and_b32_e32 v42, 0xffff0000, v234
	s_waitcnt vmcnt(7)
	v_and_b32_e32 v43, 0xffff0000, v236
	v_lshlrev_b32_e32 v41, 16, v236
	v_lshlrev_b32_e32 v40, 16, v234
	v_lshlrev_b32_e32 v44, 16, v235
	v_and_b32_e32 v46, 0xffff0000, v235
	v_pk_mul_f32 v[32:33], v[42:43], v[42:43]
	v_lshlrev_b32_e32 v45, 16, v237
	v_pk_fma_f32 v[32:33], v[40:41], v[40:41], v[32:33]
	v_and_b32_e32 v47, 0xffff0000, v237
	v_pk_fma_f32 v[32:33], v[44:45], v[44:45], v[32:33]
	s_nop 0
	v_pk_fma_f32 v[32:33], v[46:47], v[46:47], v[32:33]
	s_nop 0
	v_add_f32_e32 v32, v36, v32
	global_load_dwordx4 v[214:217], v202, s[0:1]
	global_load_dwordx4 v[218:221], v202, s[20:21]
	global_load_dwordx4 v[222:225], v[8:9], off
	v_add_f32_e32 v38, v32, v33
	s_waitcnt vmcnt(9)
	v_and_b32_e32 v32, 0xffff0000, v238
	s_waitcnt vmcnt(8)
	v_and_b32_e32 v33, 0xffff0000, v240
	v_lshlrev_b32_e32 v31, 16, v240
	v_lshlrev_b32_e32 v30, 16, v238
	v_lshlrev_b32_e32 v34, 16, v239
	v_and_b32_e32 v36, 0xffff0000, v239
	v_pk_mul_f32 v[60:61], v[32:33], v[32:33]
	v_lshlrev_b32_e32 v35, 16, v241
	v_pk_fma_f32 v[60:61], v[30:31], v[30:31], v[60:61]
	v_and_b32_e32 v37, 0xffff0000, v241
	v_pk_fma_f32 v[60:61], v[34:35], v[34:35], v[60:61]
	global_load_dwordx2 v[226:227], v[252:253], off offset:2560
	global_load_dwordx2 v[228:229], v[252:253], off offset:3072
	global_load_dwordx2 v[230:231], v[252:253], off offset:3584
	s_waitcnt vmcnt(4)
	v_pk_add_f32 v[218:219], v[218:219], 1.0 op_sel_hi:[1,0]
	v_pk_fma_f32 v[60:61], v[36:37], v[36:37], v[60:61]
	s_nop 0
	v_add_f32_e32 v38, v38, v60
	v_add_f32_e32 v38, v38, v61
	ds_bpermute_b32 v60, v189, v38
	s_waitcnt lgkmcnt(0)
	v_add_f32_e32 v38, v38, v60
	ds_bpermute_b32 v60, v192, v38
	s_waitcnt lgkmcnt(0)
	v_add_f32_e32 v38, v38, v60
	ds_bpermute_b32 v60, v193, v38
	s_waitcnt lgkmcnt(0)
	v_add_f32_e32 v38, v38, v60
	ds_bpermute_b32 v60, v194, v38
	s_waitcnt lgkmcnt(0)
	v_add_f32_e32 v38, v38, v60
	ds_bpermute_b32 v60, v195, v38
	s_waitcnt lgkmcnt(0)
	v_add_f32_e32 v38, v38, v60
	ds_bpermute_b32 v60, v196, v38
	s_waitcnt lgkmcnt(0)
	v_add_f32_e32 v38, v38, v60
	v_fmamk_f32 v38, v38, 0x3a000000, v201
	v_cmp_gt_f32_e32 vcc, s27, v38
	v_mul_f32_e32 v60, 0x4b800000, v38
	s_nop 0
	v_cndmask_b32_e32 v38, v38, v60, vcc
	v_rsq_f32_e32 v38, v38
	s_nop 0
	v_mul_f32_e32 v60, 0x45800000, v38
	v_cndmask_b32_e32 v38, v38, v60, vcc
	v_pk_mul_f32 v[2:3], v[2:3], v[38:39] op_sel_hi:[1,0]
	v_pk_mul_f32 v[4:5], v[4:5], v[38:39] op_sel_hi:[1,0]
	s_waitcnt vmcnt(3)
	v_pk_mul_f32 v[2:3], v[222:223], v[2:3]
	v_pk_mul_f32 v[4:5], v[224:225], v[4:5]
	v_pk_fma_f32 v[2:3], v[218:219], v[2:3], v[214:215]
	v_mov_b32_e32 v214, 0
	v_cvt_pk_fp8_f32 v214, v2, v3
	v_pk_add_f32 v[60:61], v[220:221], 1.0 op_sel_hi:[1,0]
	v_pk_mul_f32 v[56:57], v[56:57], v[38:39] op_sel_hi:[1,0]
	v_pk_fma_f32 v[4:5], v[60:61], v[4:5], v[216:217]
	v_lshl_add_u64 v[60:61], s[76:77], 0, v[26:27]
	v_cvt_pk_fp8_f32 v214, v4, v5 op_sel:[0,0,1]
	v_add_co_u32_e32 v60, vcc, s28, v60
	ds_write_b128 v199, v[2:5]
	s_nop 0
	v_addc_co_u32_e32 v61, vcc, 0, v61, vcc
	global_store_dword v[60:61], v214, off
	global_load_dwordx4 v[2:5], v203, s[0:1]
	s_nop 0
	global_load_dwordx4 v[214:217], v203, s[20:21]
	global_load_dwordx4 v[218:221], v[8:9], off offset:1024
	v_pk_mul_f32 v[58:59], v[58:59], v[38:39] op_sel_hi:[1,0]
	v_pk_mul_f32 v[52:53], v[52:53], v[38:39] op_sel_hi:[1,0]
	v_pk_mul_f32 v[54:55], v[54:55], v[38:39] op_sel_hi:[1,0]
	v_pk_mul_f32 v[48:49], v[48:49], v[38:39] op_sel_hi:[1,0]
	v_pk_mul_f32 v[50:51], v[50:51], v[38:39] op_sel_hi:[1,0]
	s_waitcnt vmcnt(1)
	v_pk_add_f32 v[214:215], v[214:215], 1.0 op_sel_hi:[1,0]
	s_waitcnt vmcnt(0)
	v_pk_mul_f32 v[56:57], v[218:219], v[56:57]
	v_pk_mul_f32 v[58:59], v[220:221], v[58:59]
	v_pk_fma_f32 v[2:3], v[214:215], v[56:57], v[2:3]
	v_mov_b32_e32 v56, 0
	v_cvt_pk_fp8_f32 v56, v2, v3
	v_pk_add_f32 v[216:217], v[216:217], 1.0 op_sel_hi:[1,0]
	s_nop 0
	v_pk_fma_f32 v[4:5], v[216:217], v[58:59], v[4:5]
	ds_write_b128 v199, v[2:5] offset:1024
	v_cvt_pk_fp8_f32 v56, v4, v5 op_sel:[0,0,1]
	global_store_dword v[60:61], v56, off offset:256
	global_load_dwordx4 v[2:5], v204, s[0:1]
	s_nop 0
	global_load_dwordx4 v[56:59], v204, s[20:21]
	global_load_dwordx4 v[214:217], v[8:9], off offset:2048
	s_waitcnt vmcnt(1)
	v_pk_add_f32 v[56:57], v[56:57], 1.0 op_sel_hi:[1,0]
	s_waitcnt vmcnt(0)
	v_pk_mul_f32 v[52:53], v[214:215], v[52:53]
	v_pk_mul_f32 v[54:55], v[216:217], v[54:55]
	v_pk_fma_f32 v[2:3], v[56:57], v[52:53], v[2:3]
	v_mov_b32_e32 v52, 0
	v_cvt_pk_fp8_f32 v52, v2, v3
	v_pk_add_f32 v[58:59], v[58:59], 1.0 op_sel_hi:[1,0]
	s_nop 0
	v_pk_fma_f32 v[4:5], v[58:59], v[54:55], v[4:5]
	ds_write_b128 v199, v[2:5] offset:2048
	v_cvt_pk_fp8_f32 v52, v4, v5 op_sel:[0,0,1]
	global_store_dword v[60:61], v52, off offset:512
	global_load_dwordx4 v[2:5], v205, s[0:1]
	s_nop 0
	global_load_dwordx4 v[52:55], v205, s[20:21]
	global_load_dwordx4 v[56:59], v[8:9], off offset:3072
	s_waitcnt vmcnt(1)
	v_pk_add_f32 v[52:53], v[52:53], 1.0 op_sel_hi:[1,0]
	s_waitcnt vmcnt(0)
	v_pk_mul_f32 v[48:49], v[48:49], v[56:57]
	v_pk_mul_f32 v[50:51], v[50:51], v[58:59]
	v_pk_fma_f32 v[2:3], v[52:53], v[48:49], v[2:3]
	v_mov_b32_e32 v48, 0
	v_cvt_pk_fp8_f32 v48, v2, v3
	v_pk_add_f32 v[54:55], v[54:55], 1.0 op_sel_hi:[1,0]
	v_mov_b32_e32 v58, v40
	v_pk_fma_f32 v[4:5], v[54:55], v[50:51], v[4:5]
	ds_write_b128 v199, v[2:5] offset:3072
	v_cvt_pk_fp8_f32 v48, v4, v5 op_sel:[0,0,1]
	v_mov_b32_e32 v59, v42
	v_pk_mul_f32 v[58:59], v[58:59], v[38:39] op_sel_hi:[1,0]
	v_mov_b32_e32 v40, 0
	global_store_dword v[60:61], v48, off offset:768
	global_load_dwordx4 v[2:5], v206, s[0:1]
	s_nop 0
	global_load_dwordx4 v[48:51], v206, s[20:21]
	global_load_dwordx4 v[52:55], v[10:11], off
	v_mov_b32_e32 v56, v44
	v_mov_b32_e32 v57, v46
	v_pk_mul_f32 v[56:57], v[56:57], v[38:39] op_sel_hi:[1,0]
	v_mov_b32_e32 v42, v41
	v_mov_b32_e32 v46, v45
	v_pk_mul_f32 v[44:45], v[46:47], v[38:39] op_sel_hi:[1,0]
	s_waitcnt vmcnt(1)
	v_pk_add_f32 v[48:49], v[48:49], 1.0 op_sel_hi:[1,0]
	s_waitcnt vmcnt(0)
	v_pk_mul_f32 v[52:53], v[58:59], v[52:53]
	v_pk_mul_f32 v[54:55], v[56:57], v[54:55]
	v_pk_fma_f32 v[2:3], v[48:49], v[52:53], v[2:3]
	v_pk_add_f32 v[50:51], v[50:51], 1.0 op_sel_hi:[1,0]
	v_cvt_pk_fp8_f32 v40, v2, v3
	v_pk_fma_f32 v[4:5], v[50:51], v[54:55], v[4:5]
	ds_write_b128 v199, v[2:5] offset:4096
	v_cvt_pk_fp8_f32 v40, v4, v5 op_sel:[0,0,1]
	global_store_dword v[60:61], v40, off offset:1024
	global_load_dwordx4 v[2:5], v207, s[0:1]
	global_load_dwordx4 v[48:51], v207, s[20:21]
	global_load_dwordx4 v[52:55], v[12:13], off
	v_pk_mul_f32 v[40:41], v[42:43], v[38:39] op_sel_hi:[1,0]
	s_waitcnt vmcnt(1)
	v_pk_add_f32 v[46:47], v[48:49], 1.0 op_sel_hi:[1,0]
	s_waitcnt vmcnt(0)
	v_pk_mul_f32 v[40:41], v[40:41], v[52:53]
	v_pk_mul_f32 v[42:43], v[44:45], v[54:55]
	v_pk_fma_f32 v[2:3], v[46:47], v[40:41], v[2:3]
	v_mov_b32_e32 v40, 0
	v_cvt_pk_fp8_f32 v40, v2, v3
	v_pk_add_f32 v[44:45], v[50:51], 1.0 op_sel_hi:[1,0]
	v_mov_b32_e32 v50, v30
	v_pk_fma_f32 v[4:5], v[44:45], v[42:43], v[4:5]
	ds_write_b128 v199, v[2:5] offset:5120
	v_cvt_pk_fp8_f32 v40, v4, v5 op_sel:[0,0,1]
	v_mov_b32_e32 v51, v32
	v_pk_mul_f32 v[50:51], v[50:51], v[38:39] op_sel_hi:[1,0]
	v_mov_b32_e32 v30, 0
	global_store_dword v[60:61], v40, off offset:1280
	global_load_dwordx4 v[2:5], v208, s[0:1]
	s_nop 0
	global_load_dwordx4 v[40:43], v208, s[20:21]
	global_load_dwordx4 v[44:47], v[14:15], off
	v_mov_b32_e32 v48, v34
	v_mov_b32_e32 v49, v36
	v_pk_mul_f32 v[48:49], v[48:49], v[38:39] op_sel_hi:[1,0]
	v_mov_b32_e32 v32, v31
	v_mov_b32_e32 v36, v35
	v_pk_mul_f32 v[34:35], v[36:37], v[38:39] op_sel_hi:[1,0]
	s_waitcnt vmcnt(1)
	v_pk_add_f32 v[40:41], v[40:41], 1.0 op_sel_hi:[1,0]
	s_waitcnt vmcnt(0)
	v_pk_mul_f32 v[44:45], v[50:51], v[44:45]
	v_pk_mul_f32 v[46:47], v[48:49], v[46:47]
	v_pk_fma_f32 v[2:3], v[40:41], v[44:45], v[2:3]
	v_pk_add_f32 v[42:43], v[42:43], 1.0 op_sel_hi:[1,0]
	v_cvt_pk_fp8_f32 v30, v2, v3
	v_pk_fma_f32 v[4:5], v[42:43], v[46:47], v[4:5]
	ds_write_b128 v199, v[2:5] offset:6144
	v_cvt_pk_fp8_f32 v30, v4, v5 op_sel:[0,0,1]
	global_store_dword v[60:61], v30, off offset:1536
	global_load_dwordx4 v[2:5], v209, s[0:1]
	global_load_dwordx4 v[40:43], v209, s[20:21]
	global_load_dwordx4 v[44:47], v[16:17], off
	v_pk_mul_f32 v[30:31], v[32:33], v[38:39] op_sel_hi:[1,0]
	s_add_i32 s0, s22, 1
	s_ashr_i32 s1, s0, 31
	s_lshl_b64 s[20:21], s[0:1], 12
	s_lshl_b64 s[22:23], s[0:1], 11
	s_ashr_i32 s0, s0, 13
	s_mulk_i32 s0, 0x3000
	s_ashr_i32 s1, s0, 31
	s_lshl_b64 s[0:1], s[0:1], 2
	s_waitcnt vmcnt(1)
	v_pk_add_f32 v[36:37], v[40:41], 1.0 op_sel_hi:[1,0]
	s_waitcnt vmcnt(0)
	v_pk_mul_f32 v[30:31], v[30:31], v[44:45]
	v_pk_mul_f32 v[32:33], v[34:35], v[46:47]
	v_pk_fma_f32 v[2:3], v[36:37], v[30:31], v[2:3]
	v_mov_b32_e32 v30, 0
	v_cvt_pk_fp8_f32 v30, v2, v3
	v_pk_add_f32 v[34:35], v[42:43], 1.0 op_sel_hi:[1,0]
	s_nop 0
	v_pk_fma_f32 v[4:5], v[34:35], v[32:33], v[4:5]
	ds_write_b128 v199, v[2:5] offset:7168
	v_cvt_pk_fp8_f32 v30, v4, v5 op_sel:[0,0,1]
	global_store_dword v[60:61], v30, off offset:1792
	v_lshl_add_u64 v[30:31], v[22:23], 0, s[20:21]
	s_add_u32 s20, s3, s0
	s_addc_u32 s21, s24, s1
	s_add_u32 s0, s20, 0x6000
	s_addc_u32 s1, s21, 0
	s_add_u32 s20, s20, 0x8000
	s_addc_u32 s21, s21, 0
	v_and_b32_e32 v3, 0xffff0000, v242
	v_and_b32_e32 v57, 0xffff0000, v244
	v_lshlrev_b32_e32 v2, 16, v242
	v_mul_f32_e32 v34, v3, v3
	v_lshlrev_b32_e32 v56, 16, v244
	v_mul_f32_e32 v32, v57, v57
	v_lshlrev_b32_e32 v4, 16, v243
	v_fmac_f32_e32 v34, v2, v2
	v_lshlrev_b32_e32 v58, 16, v245
	v_fmac_f32_e32 v32, v56, v56
	v_and_b32_e32 v5, 0xffff0000, v243
	v_fmac_f32_e32 v34, v4, v4
	v_and_b32_e32 v59, 0xffff0000, v245
	v_fmac_f32_e32 v32, v58, v58
	v_fmac_f32_e32 v34, v5, v5
	v_fmac_f32_e32 v32, v59, v59
	v_add_f32_e32 v34, v34, v32
	v_and_b32_e32 v53, 0xffff0000, v246
	v_lshlrev_b32_e32 v52, 16, v246
	v_mul_f32_e32 v32, v53, v53
	v_lshlrev_b32_e32 v54, 16, v247
	v_fmac_f32_e32 v32, v52, v52
	v_and_b32_e32 v55, 0xffff0000, v247
	v_fmac_f32_e32 v32, v54, v54
	v_fmac_f32_e32 v32, v55, v55
	v_add_f32_e32 v34, v34, v32
	v_and_b32_e32 v49, 0xffff0000, v248
	v_lshlrev_b32_e32 v48, 16, v248
	v_mul_f32_e32 v32, v49, v49
	v_lshlrev_b32_e32 v50, 16, v249
	v_fmac_f32_e32 v32, v48, v48
	v_and_b32_e32 v51, 0xffff0000, v249
	v_fmac_f32_e32 v32, v50, v50
	v_fmac_f32_e32 v32, v51, v51
	v_add_f32_e32 v36, v34, v32
	v_and_b32_e32 v42, 0xffff0000, v250
	v_and_b32_e32 v43, 0xffff0000, v226
	v_lshlrev_b32_e32 v41, 16, v226
	v_lshlrev_b32_e32 v40, 16, v250
	v_lshlrev_b32_e32 v44, 16, v251
	v_and_b32_e32 v46, 0xffff0000, v251
	v_pk_mul_f32 v[32:33], v[42:43], v[42:43]
	v_lshlrev_b32_e32 v45, 16, v227
	v_pk_fma_f32 v[32:33], v[40:41], v[40:41], v[32:33]
	v_and_b32_e32 v47, 0xffff0000, v227
	v_pk_fma_f32 v[32:33], v[44:45], v[44:45], v[32:33]
	s_nop 0
	v_pk_fma_f32 v[32:33], v[46:47], v[46:47], v[32:33]
	s_nop 0
	v_add_f32_e32 v32, v36, v32
	global_load_dwordx4 v[214:217], v202, s[0:1]
	global_load_dwordx4 v[218:221], v202, s[20:21]
	global_load_dwordx4 v[222:225], v[8:9], off
	v_add_f32_e32 v38, v32, v33
	s_waitcnt vmcnt(4)
	v_and_b32_e32 v32, 0xffff0000, v228
	s_waitcnt vmcnt(3)
	v_and_b32_e32 v33, 0xffff0000, v230
	v_lshlrev_b32_e32 v31, 16, v230
	v_lshlrev_b32_e32 v30, 16, v228
	v_lshlrev_b32_e32 v34, 16, v229
	v_and_b32_e32 v36, 0xffff0000, v229
	v_pk_mul_f32 v[60:61], v[32:33], v[32:33]
	v_lshlrev_b32_e32 v35, 16, v231
	v_pk_fma_f32 v[60:61], v[30:31], v[30:31], v[60:61]
	v_and_b32_e32 v37, 0xffff0000, v231
	v_pk_fma_f32 v[60:61], v[34:35], v[34:35], v[60:61]
	s_waitcnt vmcnt(1)
	v_pk_add_f32 v[218:219], v[218:219], 1.0 op_sel_hi:[1,0]
	v_pk_fma_f32 v[60:61], v[36:37], v[36:37], v[60:61]
	s_nop 0
	v_add_f32_e32 v38, v38, v60
	v_add_f32_e32 v38, v38, v61
	ds_bpermute_b32 v60, v189, v38
	s_waitcnt lgkmcnt(0)
	v_add_f32_e32 v38, v38, v60
	ds_bpermute_b32 v60, v192, v38
	s_waitcnt lgkmcnt(0)
	v_add_f32_e32 v38, v38, v60
	ds_bpermute_b32 v60, v193, v38
	s_waitcnt lgkmcnt(0)
	v_add_f32_e32 v38, v38, v60
	ds_bpermute_b32 v60, v194, v38
	s_waitcnt lgkmcnt(0)
	v_add_f32_e32 v38, v38, v60
	ds_bpermute_b32 v60, v195, v38
	s_waitcnt lgkmcnt(0)
	v_add_f32_e32 v38, v38, v60
	ds_bpermute_b32 v60, v196, v38
	s_waitcnt lgkmcnt(0)
	v_add_f32_e32 v38, v38, v60
	v_fmamk_f32 v38, v38, 0x3a000000, v201
	v_cmp_gt_f32_e32 vcc, s27, v38
	v_mul_f32_e32 v60, 0x4b800000, v38
	s_nop 0
	v_cndmask_b32_e32 v38, v38, v60, vcc
	v_rsq_f32_e32 v38, v38
	s_nop 0
	v_mul_f32_e32 v60, 0x45800000, v38
	v_cndmask_b32_e32 v38, v38, v60, vcc
	v_pk_mul_f32 v[2:3], v[2:3], v[38:39] op_sel_hi:[1,0]
	v_pk_mul_f32 v[4:5], v[4:5], v[38:39] op_sel_hi:[1,0]
	s_waitcnt vmcnt(0)
	v_pk_mul_f32 v[2:3], v[222:223], v[2:3]
	v_pk_mul_f32 v[4:5], v[224:225], v[4:5]
	v_pk_fma_f32 v[2:3], v[218:219], v[2:3], v[214:215]
	v_mov_b32_e32 v214, 0
	v_cvt_pk_fp8_f32 v214, v2, v3
	v_pk_add_f32 v[60:61], v[220:221], 1.0 op_sel_hi:[1,0]
	v_pk_mul_f32 v[56:57], v[56:57], v[38:39] op_sel_hi:[1,0]
	v_pk_fma_f32 v[4:5], v[60:61], v[4:5], v[216:217]
	v_lshl_add_u64 v[60:61], v[24:25], 0, s[22:23]
	v_cvt_pk_fp8_f32 v214, v4, v5 op_sel:[0,0,1]
	ds_write_b128 v200, v[2:5]
	v_pk_mul_f32 v[58:59], v[58:59], v[38:39] op_sel_hi:[1,0]
	v_pk_mul_f32 v[52:53], v[52:53], v[38:39] op_sel_hi:[1,0]
	global_store_dword v[60:61], v214, off
	global_load_dwordx4 v[2:5], v203, s[0:1]
	s_nop 0
	global_load_dwordx4 v[214:217], v203, s[20:21]
	global_load_dwordx4 v[218:221], v[8:9], off offset:1024
	v_pk_mul_f32 v[54:55], v[54:55], v[38:39] op_sel_hi:[1,0]
	v_pk_mul_f32 v[48:49], v[48:49], v[38:39] op_sel_hi:[1,0]
	v_pk_mul_f32 v[50:51], v[50:51], v[38:39] op_sel_hi:[1,0]
	s_waitcnt vmcnt(1)
	v_pk_add_f32 v[214:215], v[214:215], 1.0 op_sel_hi:[1,0]
	s_waitcnt vmcnt(0)
	v_pk_mul_f32 v[56:57], v[218:219], v[56:57]
	v_pk_mul_f32 v[58:59], v[220:221], v[58:59]
	v_pk_fma_f32 v[2:3], v[214:215], v[56:57], v[2:3]
	v_mov_b32_e32 v56, 0
	v_cvt_pk_fp8_f32 v56, v2, v3
	v_pk_add_f32 v[216:217], v[216:217], 1.0 op_sel_hi:[1,0]
	s_nop 0
	v_pk_fma_f32 v[4:5], v[216:217], v[58:59], v[4:5]
	ds_write_b128 v200, v[2:5] offset:1024
	v_cvt_pk_fp8_f32 v56, v4, v5 op_sel:[0,0,1]
	global_store_dword v[60:61], v56, off offset:256
	global_load_dwordx4 v[2:5], v204, s[0:1]
	s_nop 0
	global_load_dwordx4 v[56:59], v204, s[20:21]
	global_load_dwordx4 v[214:217], v[8:9], off offset:2048
	s_waitcnt vmcnt(1)
	v_pk_add_f32 v[56:57], v[56:57], 1.0 op_sel_hi:[1,0]
	s_waitcnt vmcnt(0)
	v_pk_mul_f32 v[52:53], v[214:215], v[52:53]
	v_pk_mul_f32 v[54:55], v[216:217], v[54:55]
	v_pk_fma_f32 v[2:3], v[56:57], v[52:53], v[2:3]
	v_mov_b32_e32 v52, 0
	v_cvt_pk_fp8_f32 v52, v2, v3
	v_pk_add_f32 v[58:59], v[58:59], 1.0 op_sel_hi:[1,0]
	s_nop 0
	v_pk_fma_f32 v[4:5], v[58:59], v[54:55], v[4:5]
	ds_write_b128 v200, v[2:5] offset:2048
	v_cvt_pk_fp8_f32 v52, v4, v5 op_sel:[0,0,1]
	global_store_dword v[60:61], v52, off offset:512
	global_load_dwordx4 v[2:5], v205, s[0:1]
	s_nop 0
	global_load_dwordx4 v[52:55], v205, s[20:21]
	global_load_dwordx4 v[56:59], v[8:9], off offset:3072
	s_waitcnt vmcnt(1)
	v_pk_add_f32 v[52:53], v[52:53], 1.0 op_sel_hi:[1,0]
	s_waitcnt vmcnt(0)
	v_pk_mul_f32 v[48:49], v[48:49], v[56:57]
	v_pk_mul_f32 v[50:51], v[50:51], v[58:59]
	v_pk_fma_f32 v[2:3], v[52:53], v[48:49], v[2:3]
	v_mov_b32_e32 v48, 0
	v_cvt_pk_fp8_f32 v48, v2, v3
	v_pk_add_f32 v[54:55], v[54:55], 1.0 op_sel_hi:[1,0]
	v_mov_b32_e32 v58, v40
	v_pk_fma_f32 v[4:5], v[54:55], v[50:51], v[4:5]
	ds_write_b128 v200, v[2:5] offset:3072
	v_cvt_pk_fp8_f32 v48, v4, v5 op_sel:[0,0,1]
	v_mov_b32_e32 v59, v42
	v_pk_mul_f32 v[58:59], v[58:59], v[38:39] op_sel_hi:[1,0]
	v_mov_b32_e32 v40, 0
	global_store_dword v[60:61], v48, off offset:768
	global_load_dwordx4 v[2:5], v206, s[0:1]
	s_nop 0
	global_load_dwordx4 v[48:51], v206, s[20:21]
	global_load_dwordx4 v[52:55], v[10:11], off
	v_mov_b32_e32 v56, v44
	v_mov_b32_e32 v57, v46
	v_pk_mul_f32 v[56:57], v[56:57], v[38:39] op_sel_hi:[1,0]
	v_mov_b32_e32 v42, v41
	v_mov_b32_e32 v46, v45
	v_pk_mul_f32 v[44:45], v[46:47], v[38:39] op_sel_hi:[1,0]
	s_waitcnt vmcnt(1)
	v_pk_add_f32 v[48:49], v[48:49], 1.0 op_sel_hi:[1,0]
	s_waitcnt vmcnt(0)
	v_pk_mul_f32 v[52:53], v[58:59], v[52:53]
	v_pk_mul_f32 v[54:55], v[56:57], v[54:55]
	v_pk_fma_f32 v[2:3], v[48:49], v[52:53], v[2:3]
	v_pk_add_f32 v[50:51], v[50:51], 1.0 op_sel_hi:[1,0]
	v_cvt_pk_fp8_f32 v40, v2, v3
	v_pk_fma_f32 v[4:5], v[50:51], v[54:55], v[4:5]
	ds_write_b128 v200, v[2:5] offset:4096
	v_cvt_pk_fp8_f32 v40, v4, v5 op_sel:[0,0,1]
	global_store_dword v[60:61], v40, off offset:1024
	global_load_dwordx4 v[2:5], v207, s[0:1]
	global_load_dwordx4 v[48:51], v207, s[20:21]
	global_load_dwordx4 v[52:55], v[12:13], off
	v_pk_mul_f32 v[40:41], v[42:43], v[38:39] op_sel_hi:[1,0]
	s_waitcnt vmcnt(1)
	v_pk_add_f32 v[46:47], v[48:49], 1.0 op_sel_hi:[1,0]
	s_waitcnt vmcnt(0)
	v_pk_mul_f32 v[40:41], v[40:41], v[52:53]
	v_pk_mul_f32 v[42:43], v[44:45], v[54:55]
	v_pk_fma_f32 v[2:3], v[46:47], v[40:41], v[2:3]
	v_mov_b32_e32 v40, 0
	v_cvt_pk_fp8_f32 v40, v2, v3
	v_pk_add_f32 v[44:45], v[50:51], 1.0 op_sel_hi:[1,0]
	v_mov_b32_e32 v50, v30
	v_pk_fma_f32 v[4:5], v[44:45], v[42:43], v[4:5]
	ds_write_b128 v200, v[2:5] offset:5120
	v_cvt_pk_fp8_f32 v40, v4, v5 op_sel:[0,0,1]
	v_mov_b32_e32 v51, v32
	v_pk_mul_f32 v[50:51], v[50:51], v[38:39] op_sel_hi:[1,0]
	v_mov_b32_e32 v30, 0
	global_store_dword v[60:61], v40, off offset:1280
	global_load_dwordx4 v[2:5], v208, s[0:1]
	s_nop 0
	global_load_dwordx4 v[40:43], v208, s[20:21]
	global_load_dwordx4 v[44:47], v[14:15], off
	v_mov_b32_e32 v48, v34
	v_mov_b32_e32 v49, v36
	v_pk_mul_f32 v[48:49], v[48:49], v[38:39] op_sel_hi:[1,0]
	v_mov_b32_e32 v32, v31
	v_mov_b32_e32 v36, v35
	v_pk_mul_f32 v[34:35], v[36:37], v[38:39] op_sel_hi:[1,0]
	s_waitcnt vmcnt(1)
	v_pk_add_f32 v[40:41], v[40:41], 1.0 op_sel_hi:[1,0]
	s_waitcnt vmcnt(0)
	v_pk_mul_f32 v[44:45], v[50:51], v[44:45]
	v_pk_mul_f32 v[46:47], v[48:49], v[46:47]
	v_pk_fma_f32 v[2:3], v[40:41], v[44:45], v[2:3]
	v_pk_add_f32 v[42:43], v[42:43], 1.0 op_sel_hi:[1,0]
	v_cvt_pk_fp8_f32 v30, v2, v3
	v_pk_fma_f32 v[4:5], v[42:43], v[46:47], v[4:5]
	ds_write_b128 v200, v[2:5] offset:6144
	v_cvt_pk_fp8_f32 v30, v4, v5 op_sel:[0,0,1]
	global_store_dword v[60:61], v30, off offset:1536
	global_load_dwordx4 v[2:5], v209, s[0:1]
	global_load_dwordx4 v[40:43], v209, s[20:21]
	global_load_dwordx4 v[44:47], v[16:17], off
	v_pk_mul_f32 v[30:31], v[32:33], v[38:39] op_sel_hi:[1,0]
	s_waitcnt vmcnt(1)
	v_pk_add_f32 v[36:37], v[40:41], 1.0 op_sel_hi:[1,0]
	s_waitcnt vmcnt(0)
	v_pk_mul_f32 v[30:31], v[30:31], v[44:45]
	v_pk_mul_f32 v[32:33], v[34:35], v[46:47]
	v_pk_fma_f32 v[2:3], v[36:37], v[30:31], v[2:3]
	v_mov_b32_e32 v30, 0
	v_cvt_pk_fp8_f32 v30, v2, v3
	v_pk_add_f32 v[34:35], v[42:43], 1.0 op_sel_hi:[1,0]
	s_nop 0
	v_pk_fma_f32 v[4:5], v[34:35], v[32:33], v[4:5]
	ds_write_b128 v200, v[2:5] offset:7168
	v_cvt_pk_fp8_f32 v30, v4, v5 op_sel:[0,0,1]
	global_store_dword v[60:61], v30, off offset:1792
	s_waitcnt lgkmcnt(0)
	s_barrier
	ds_read_b128 v[2:5], v210
	s_waitcnt lgkmcnt(0)
	v_mfma_f32_16x16x4_f32 v[30:33], v2, v1, 0
	v_mfma_f32_16x16x4_f32 v[34:37], v2, v39, 0
	v_mfma_f32_16x16x4_f32 v[30:33], v3, v62, v[30:33]
	v_mfma_f32_16x16x4_f32 v[34:37], v3, v63, v[34:37]
	v_mfma_f32_16x16x4_f32 v[30:33], v4, v64, v[30:33]
	v_mfma_f32_16x16x4_f32 v[34:37], v4, v65, v[34:37]
	v_mfma_f32_16x16x4_f32 v[30:33], v5, v66, v[30:33]
	v_mfma_f32_16x16x4_f32 v[2:5], v5, v67, v[34:37]
	s_nop 7
	ds_read_b128 v[34:37], v210 offset:64
	s_waitcnt lgkmcnt(0)
	v_mfma_f32_16x16x4_f32 v[30:33], v34, v68, v[30:33]
	v_mfma_f32_16x16x4_f32 v[2:5], v34, v69, v[2:5]
	v_mfma_f32_16x16x4_f32 v[30:33], v35, v70, v[30:33]
	v_mfma_f32_16x16x4_f32 v[2:5], v35, v71, v[2:5]
	v_mfma_f32_16x16x4_f32 v[30:33], v36, v72, v[30:33]
	v_mfma_f32_16x16x4_f32 v[2:5], v36, v73, v[2:5]
	v_mfma_f32_16x16x4_f32 v[30:33], v37, v74, v[30:33]
	v_mfma_f32_16x16x4_f32 v[2:5], v37, v75, v[2:5]
	ds_read_b128 v[34:37], v210 offset:128
	s_waitcnt lgkmcnt(0)
	v_mfma_f32_16x16x4_f32 v[30:33], v34, v76, v[30:33]
	v_mfma_f32_16x16x4_f32 v[2:5], v34, v77, v[2:5]
	v_mfma_f32_16x16x4_f32 v[30:33], v35, v78, v[30:33]
	v_mfma_f32_16x16x4_f32 v[2:5], v35, v79, v[2:5]
	v_mfma_f32_16x16x4_f32 v[30:33], v36, v80, v[30:33]
	v_mfma_f32_16x16x4_f32 v[2:5], v36, v81, v[2:5]
	v_mfma_f32_16x16x4_f32 v[30:33], v37, v82, v[30:33]
	v_mfma_f32_16x16x4_f32 v[2:5], v37, v83, v[2:5]
	ds_read_b128 v[34:37], v210 offset:192
	s_waitcnt lgkmcnt(0)
	v_mfma_f32_16x16x4_f32 v[30:33], v34, v84, v[30:33]
	v_mfma_f32_16x16x4_f32 v[2:5], v34, v85, v[2:5]
	v_mfma_f32_16x16x4_f32 v[30:33], v35, v86, v[30:33]
	v_mfma_f32_16x16x4_f32 v[2:5], v35, v87, v[2:5]
	v_mfma_f32_16x16x4_f32 v[30:33], v36, v88, v[30:33]
	v_mfma_f32_16x16x4_f32 v[2:5], v36, v89, v[2:5]
	v_mfma_f32_16x16x4_f32 v[30:33], v37, v90, v[30:33]
	v_mfma_f32_16x16x4_f32 v[2:5], v37, v91, v[2:5]
	ds_read_b128 v[34:37], v210 offset:256
	s_waitcnt lgkmcnt(0)
	v_mfma_f32_16x16x4_f32 v[30:33], v34, v92, v[30:33]
	v_mfma_f32_16x16x4_f32 v[2:5], v34, v93, v[2:5]
	v_mfma_f32_16x16x4_f32 v[30:33], v35, v94, v[30:33]
	v_mfma_f32_16x16x4_f32 v[2:5], v35, v95, v[2:5]
	v_mfma_f32_16x16x4_f32 v[30:33], v36, v96, v[30:33]
	v_mfma_f32_16x16x4_f32 v[2:5], v36, v97, v[2:5]
	v_mfma_f32_16x16x4_f32 v[30:33], v37, v98, v[30:33]
	v_mfma_f32_16x16x4_f32 v[2:5], v37, v99, v[2:5]
	ds_read_b128 v[34:37], v210 offset:320
	s_waitcnt lgkmcnt(0)
	v_mfma_f32_16x16x4_f32 v[30:33], v34, v100, v[30:33]
	v_mfma_f32_16x16x4_f32 v[2:5], v34, v101, v[2:5]
	v_mfma_f32_16x16x4_f32 v[30:33], v35, v102, v[30:33]
	v_mfma_f32_16x16x4_f32 v[2:5], v35, v103, v[2:5]
	v_mfma_f32_16x16x4_f32 v[30:33], v36, v104, v[30:33]
	v_mfma_f32_16x16x4_f32 v[2:5], v36, v105, v[2:5]
	v_mfma_f32_16x16x4_f32 v[30:33], v37, v106, v[30:33]
	v_mfma_f32_16x16x4_f32 v[2:5], v37, v107, v[2:5]
	ds_read_b128 v[34:37], v210 offset:384
	s_waitcnt lgkmcnt(0)
	v_mfma_f32_16x16x4_f32 v[30:33], v34, v108, v[30:33]
	v_mfma_f32_16x16x4_f32 v[2:5], v34, v109, v[2:5]
	v_mfma_f32_16x16x4_f32 v[30:33], v35, v110, v[30:33]
	v_mfma_f32_16x16x4_f32 v[2:5], v35, v111, v[2:5]
	v_mfma_f32_16x16x4_f32 v[30:33], v36, v112, v[30:33]
	v_mfma_f32_16x16x4_f32 v[2:5], v36, v113, v[2:5]
	v_mfma_f32_16x16x4_f32 v[30:33], v37, v114, v[30:33]
	v_mfma_f32_16x16x4_f32 v[2:5], v37, v115, v[2:5]
	ds_read_b128 v[34:37], v210 offset:448
	s_waitcnt lgkmcnt(0)
	v_mfma_f32_16x16x4_f32 v[30:33], v34, v116, v[30:33]
	v_mfma_f32_16x16x4_f32 v[2:5], v34, v117, v[2:5]
	v_mfma_f32_16x16x4_f32 v[30:33], v35, v118, v[30:33]
	v_mfma_f32_16x16x4_f32 v[2:5], v35, v119, v[2:5]
	v_mfma_f32_16x16x4_f32 v[30:33], v36, v120, v[30:33]
	v_mfma_f32_16x16x4_f32 v[2:5], v36, v121, v[2:5]
	v_mfma_f32_16x16x4_f32 v[30:33], v37, v122, v[30:33]
	v_mfma_f32_16x16x4_f32 v[2:5], v37, v123, v[2:5]
	ds_read_b128 v[34:37], v210 offset:512
	s_waitcnt lgkmcnt(0)
	v_mfma_f32_16x16x4_f32 v[30:33], v34, v124, v[30:33]
	v_mfma_f32_16x16x4_f32 v[2:5], v34, v125, v[2:5]
	v_mfma_f32_16x16x4_f32 v[30:33], v35, v126, v[30:33]
	v_mfma_f32_16x16x4_f32 v[2:5], v35, v127, v[2:5]
	v_mfma_f32_16x16x4_f32 v[30:33], v36, v128, v[30:33]
	v_mfma_f32_16x16x4_f32 v[2:5], v36, v129, v[2:5]
	v_mfma_f32_16x16x4_f32 v[30:33], v37, v130, v[30:33]
	v_mfma_f32_16x16x4_f32 v[2:5], v37, v131, v[2:5]
	ds_read_b128 v[34:37], v210 offset:576
	s_waitcnt lgkmcnt(0)
	v_mfma_f32_16x16x4_f32 v[30:33], v34, v132, v[30:33]
	v_mfma_f32_16x16x4_f32 v[2:5], v34, v133, v[2:5]
	v_mfma_f32_16x16x4_f32 v[30:33], v35, v134, v[30:33]
	v_mfma_f32_16x16x4_f32 v[2:5], v35, v135, v[2:5]
	v_mfma_f32_16x16x4_f32 v[30:33], v36, v136, v[30:33]
	v_mfma_f32_16x16x4_f32 v[2:5], v36, v137, v[2:5]
	v_mfma_f32_16x16x4_f32 v[30:33], v37, v138, v[30:33]
	v_mfma_f32_16x16x4_f32 v[2:5], v37, v139, v[2:5]
	ds_read_b128 v[34:37], v210 offset:640
	s_waitcnt lgkmcnt(0)
	v_mfma_f32_16x16x4_f32 v[30:33], v34, v140, v[30:33]
	v_mfma_f32_16x16x4_f32 v[2:5], v34, v141, v[2:5]
	v_mfma_f32_16x16x4_f32 v[30:33], v35, v142, v[30:33]
	v_mfma_f32_16x16x4_f32 v[2:5], v35, v143, v[2:5]
	v_mfma_f32_16x16x4_f32 v[30:33], v36, v144, v[30:33]
	v_mfma_f32_16x16x4_f32 v[2:5], v36, v145, v[2:5]
	v_mfma_f32_16x16x4_f32 v[30:33], v37, v146, v[30:33]
	v_mfma_f32_16x16x4_f32 v[2:5], v37, v147, v[2:5]
	ds_read_b128 v[34:37], v210 offset:704
	s_waitcnt lgkmcnt(0)
	v_mfma_f32_16x16x4_f32 v[30:33], v34, v148, v[30:33]
	v_mfma_f32_16x16x4_f32 v[2:5], v34, v149, v[2:5]
	v_mfma_f32_16x16x4_f32 v[30:33], v35, v150, v[30:33]
	v_mfma_f32_16x16x4_f32 v[2:5], v35, v151, v[2:5]
	v_mfma_f32_16x16x4_f32 v[30:33], v36, v152, v[30:33]
	v_mfma_f32_16x16x4_f32 v[2:5], v36, v153, v[2:5]
	v_mfma_f32_16x16x4_f32 v[30:33], v37, v154, v[30:33]
	v_mfma_f32_16x16x4_f32 v[2:5], v37, v155, v[2:5]
	ds_read_b128 v[34:37], v210 offset:768
	s_waitcnt lgkmcnt(0)
	v_mfma_f32_16x16x4_f32 v[30:33], v34, v156, v[30:33]
	v_mfma_f32_16x16x4_f32 v[2:5], v34, v157, v[2:5]
	v_mfma_f32_16x16x4_f32 v[30:33], v35, v158, v[30:33]
	v_mfma_f32_16x16x4_f32 v[2:5], v35, v159, v[2:5]
	v_mfma_f32_16x16x4_f32 v[30:33], v36, v160, v[30:33]
	v_mfma_f32_16x16x4_f32 v[2:5], v36, v161, v[2:5]
	v_mfma_f32_16x16x4_f32 v[30:33], v37, v162, v[30:33]
	v_mfma_f32_16x16x4_f32 v[2:5], v37, v163, v[2:5]
	ds_read_b128 v[34:37], v210 offset:832
	s_waitcnt lgkmcnt(0)
	v_mfma_f32_16x16x4_f32 v[30:33], v34, v164, v[30:33]
	v_mfma_f32_16x16x4_f32 v[2:5], v34, v165, v[2:5]
	v_mfma_f32_16x16x4_f32 v[30:33], v35, v166, v[30:33]
	v_mfma_f32_16x16x4_f32 v[2:5], v35, v167, v[2:5]
	v_mfma_f32_16x16x4_f32 v[30:33], v36, v168, v[30:33]
	v_mfma_f32_16x16x4_f32 v[2:5], v36, v169, v[2:5]
	v_mfma_f32_16x16x4_f32 v[30:33], v37, v170, v[30:33]
	v_mfma_f32_16x16x4_f32 v[2:5], v37, v171, v[2:5]
	ds_read_b128 v[34:37], v210 offset:896
	s_waitcnt lgkmcnt(0)
	v_mfma_f32_16x16x4_f32 v[30:33], v34, v172, v[30:33]
	v_mfma_f32_16x16x4_f32 v[2:5], v34, v173, v[2:5]
	v_mfma_f32_16x16x4_f32 v[30:33], v35, v174, v[30:33]
	v_mfma_f32_16x16x4_f32 v[2:5], v35, v175, v[2:5]
	v_mfma_f32_16x16x4_f32 v[30:33], v36, v176, v[30:33]
	v_mfma_f32_16x16x4_f32 v[2:5], v36, v177, v[2:5]
	v_mfma_f32_16x16x4_f32 v[30:33], v37, v178, v[30:33]
	v_mfma_f32_16x16x4_f32 v[2:5], v37, v179, v[2:5]
	ds_read_b128 v[34:37], v210 offset:960
	s_waitcnt lgkmcnt(0)
	v_mfma_f32_16x16x4_f32 v[30:33], v34, v180, v[30:33]
	v_mfma_f32_16x16x4_f32 v[2:5], v34, v181, v[2:5]
	v_mfma_f32_16x16x4_f32 v[30:33], v35, v182, v[30:33]
	v_mfma_f32_16x16x4_f32 v[2:5], v35, v183, v[2:5]
	v_mfma_f32_16x16x4_f32 v[30:33], v36, v184, v[30:33]
	v_mfma_f32_16x16x4_f32 v[2:5], v36, v185, v[2:5]
	v_mfma_f32_16x16x4_f32 v[30:33], v37, v186, v[30:33]
	v_mfma_f32_16x16x4_f32 v[2:5], v37, v187, v[2:5]
	s_nop 9
	ds_write2_b32 v211, v30, v2 offset1:16
	ds_write2_b32 v211, v31, v3 offset0:32 offset1:48
	ds_write2_b32 v211, v32, v4 offset0:64 offset1:80
	ds_write2_b32 v211, v33, v5 offset0:96 offset1:112
	s_waitcnt lgkmcnt(0)
	s_barrier
	global_load_dword v4, v[18:19], off
	ds_read2st64_b32 v[2:3], v198 offset1:8
	ds_bpermute_b32 v31, v192, v197
	s_waitcnt vmcnt(0) lgkmcnt(1)
	v_add_f32_e32 v2, v4, v2
	v_add_f32_e32 v4, v2, v3
	ds_read2st64_b32 v[2:3], v198 offset0:16 offset1:24
	s_waitcnt lgkmcnt(0)
	v_add_f32_e32 v2, v4, v2
	v_add_f32_e32 v4, v2, v3
	ds_read2st64_b32 v[2:3], v198 offset0:32 offset1:40
	s_waitcnt lgkmcnt(0)
	v_add_f32_e32 v2, v4, v2
	v_add_f32_e32 v4, v2, v3
	ds_read2st64_b32 v[2:3], v198 offset0:48 offset1:56
	s_waitcnt lgkmcnt(0)
	v_add_f32_e32 v2, v4, v2
	v_add_f32_e32 v3, v2, v3
	ds_bpermute_b32 v5, v192, v3
	s_waitcnt lgkmcnt(0)
	v_cmp_lt_f32_e64 s[20:21], v3, v5
	v_cmp_nlt_f32_e32 vcc, v3, v5
	s_and_saveexec_b64 s[22:23], vcc
	v_cmp_eq_f32_e32 vcc, v3, v5
	v_cmp_lt_i32_e64 s[0:1], v31, v197
	s_and_b64 s[0:1], vcc, s[0:1]
	s_andn2_b64 s[20:21], s[20:21], exec
	s_and_b64 s[0:1], s[0:1], exec
	s_or_b64 s[20:21], s[20:21], s[0:1]
	s_or_b64 exec, exec, s[22:23]
	v_mov_b32_e32 v4, v3
	v_mov_b32_e32 v30, v3
	v_mov_b32_e32 v2, v197
	s_and_saveexec_b64 s[0:1], s[20:21]
	v_mov_b32_e32 v4, v5
	v_mov_b32_e32 v30, v5
	v_mov_b32_e32 v2, v31
	s_or_b64 exec, exec, s[0:1]
	ds_bpermute_b32 v5, v193, v4
	ds_bpermute_b32 v31, v193, v2
	s_waitcnt lgkmcnt(1)
	v_cmp_lt_f32_e64 s[20:21], v30, v5
	v_cmp_nlt_f32_e32 vcc, v30, v5
	s_and_saveexec_b64 s[22:23], vcc
	s_cbranch_execz .LBB0_688
	v_cmp_eq_f32_e32 vcc, v30, v5
	s_waitcnt lgkmcnt(0)
	v_cmp_lt_i32_e64 s[0:1], v31, v2
	s_and_b64 s[0:1], vcc, s[0:1]
	s_andn2_b64 s[20:21], s[20:21], exec
	s_and_b64 s[0:1], s[0:1], exec
	s_or_b64 s[20:21], s[20:21], s[0:1]
